# attention: K/V gathers in saddr form (one VALU per address), softmax max/sum butterflies via v_permlane16/32_swap instead of ds_bpermute, padding writes skipped when nsel == 256 (on top of v51)
# baseline (speedup 1.0000x reference)
.LBB0_1194:
	s_waitcnt lgkmcnt(0)
	s_min_i32 s10, s97, 0xff
	v_and_b32_e32 v210, 15, v10
	v_ashrrev_i32_e32 v211, 4, v10
	v_lshl_add_u32 v2, v10, 1, s95
	s_sub_i32 s13, s10, 63
	s_add_i32 s12, s10, 0xffffff81
	s_add_i32 s11, s10, 0xffffff41
	s_cmpk_gt_i32 s97, 0xfe
	s_cbranch_scc1 .Lpad_skip
	v_cmp_lt_i32_e32 vcc, s10, v10
	s_and_saveexec_b64 s[0:1], vcc
	ds_write_b16 v2, v141
	s_or_b64 exec, exec, s[0:1]
	s_sub_i32 s13, s10, 63
	v_cmp_le_i32_e32 vcc, s13, v10
	s_and_saveexec_b64 s[0:1], vcc
	ds_write_b16 v2, v141 offset:128
	s_or_b64 exec, exec, s[0:1]
	s_add_i32 s12, s10, 0xffffff81
	v_cmp_le_i32_e32 vcc, s12, v10
	s_and_saveexec_b64 s[0:1], vcc
	ds_write_b16 v2, v141 offset:256
	s_or_b64 exec, exec, s[0:1]
	s_add_i32 s11, s10, 0xffffff41
	v_cmp_le_i32_e32 vcc, s11, v10
	s_and_saveexec_b64 s[0:1], vcc
	ds_write_b16 v2, v141 offset:384
	s_or_b64 exec, exec, s[0:1]
.Lpad_skip:
	s_add_i32 s0, s97, s25
	s_ashr_i32 s1, s0, 31
	s_waitcnt lgkmcnt(0)
	s_lshl_b64 s[8:9], s[0:1], 10
	v_readlane_b32 s14, v254, 60
	v_lshl_add_u32 v2, v210, 1, s95
	v_ashrrev_i32_e32 v213, 3, v10
	v_and_b32_e32 v214, 7, v10
	s_add_u32 s8, s14, s8
	v_readlane_b32 s14, v254, 61
	v_and_b32_e32 v120, 7, v210
	ds_read_u16 v15, v2
	ds_read_u16 v32, v2 offset:32
	ds_read_u16 v38, v2 offset:64
	ds_read_u16 v39, v2 offset:96
	ds_read_u16 v40, v2 offset:128
	ds_read_u16 v41, v2 offset:160
	ds_read_u16 v54, v2 offset:192
	ds_read_u16 v55, v2 offset:224
	ds_read_u16 v56, v2 offset:256
	ds_read_u16 v14, v2 offset:288
	ds_read_u16 v13, v2 offset:320
	ds_read_u16 v12, v2 offset:352
	ds_read_u16 v9, v2 offset:384
	ds_read_u16 v8, v2 offset:416
	ds_read_u16 v7, v2 offset:448
	ds_read_u16 v6, v2 offset:480
	s_addc_u32 s9, s14, s9
	v_lshl_add_u32 v212, v213, 1, s95
	v_lshlrev_b32_e32 v140, 7, v120
	v_lshlrev_b32_e32 v24, 4, v211
	ds_read_u16 v5, v212
	ds_read_u16 v4, v212 offset:16
	ds_read_u16 v11, v212 offset:32
	ds_read_u16 v10, v212 offset:48
	s_waitcnt lgkmcnt(0)
	v_lshl_add_u64 v[2:3], s[8:9], 0, v[140:141]
	v_ashrrev_i32_e32 v25, 31, v24
	v_lshl_add_u64 v[2:3], v[24:25], 1, v[2:3]
	global_load_dwordx4 v[16:19], v[2:3], off
	global_load_dwordx4 v[20:23], v[2:3], off offset:16
	v_lshl_add_u64 v[2:3], s[46:47], 0, v[24:25]
	s_waitcnt lgkmcnt(0)
	v_lshl_add_u32 v244, v15, 7, v24
	global_load_dwordx4 v[156:159], v244, s[46:47]
	global_load_dwordx4 v[160:163], v244, s[46:47] offset:64
	v_lshl_add_u32 v244, v32, 7, v24
	global_load_dwordx4 v[164:167], v244, s[46:47]
	global_load_dwordx4 v[168:171], v244, s[46:47] offset:64
	v_lshl_add_u32 v244, v38, 7, v24
	global_load_dwordx4 v[172:175], v244, s[46:47]
	global_load_dwordx4 v[176:179], v244, s[46:47] offset:64
	v_lshl_add_u32 v244, v39, 7, v24
	global_load_dwordx4 v[180:183], v244, s[46:47]
	global_load_dwordx4 v[184:187], v244, s[46:47] offset:64
	v_lshl_add_u32 v244, v40, 7, v24
	global_load_dwordx4 v[188:191], v244, s[46:47]
	global_load_dwordx4 v[192:195], v244, s[46:47] offset:64
	v_lshl_add_u32 v244, v41, 7, v24
	global_load_dwordx4 v[196:199], v244, s[46:47]
	global_load_dwordx4 v[224:227], v244, s[46:47] offset:64
	v_lshl_add_u32 v244, v54, 7, v24
	global_load_dwordx4 v[228:231], v244, s[46:47]
	global_load_dwordx4 v[232:235], v244, s[46:47] offset:64
	v_lshl_add_u32 v244, v55, 7, v24
	global_load_dwordx4 v[236:239], v244, s[46:47]
	global_load_dwordx4 v[240:243], v244, s[46:47] offset:64
	v_mov_b32_e32 v15, v141
	v_mov_b32_e32 v42, v141
	v_mov_b32_e32 v43, v141
	v_mov_b32_e32 v44, v141
	v_lshlrev_b32_e32 v116, 4, v214
	v_ashrrev_i32_e32 v117, 31, v116
	v_lshl_add_u64 v[114:115], s[48:49], 0, v[116:117]
	v_lshl_add_u32 v121, v211, 3, s95
	v_lshlrev_b32_e32 v117, 2, v211
	ds_read2_b64 v[110:113], v121 offset1:4
	ds_read2_b64 v[106:109], v121 offset0:8 offset1:12
	ds_read2_b64 v[102:105], v121 offset0:16 offset1:20
	ds_read2_b64 v[98:101], v121 offset0:24 offset1:28
	ds_read2_b64 v[94:97], v121 offset0:32 offset1:36
	ds_read2_b64 v[90:93], v121 offset0:40 offset1:44
	ds_read2_b64 v[86:89], v121 offset0:48 offset1:52
	s_waitcnt vmcnt(16)
	v_lshlrev_b32_e32 v45, 16, v16
	v_and_b32_e32 v16, 0xffff0000, v16
	v_lshlrev_b32_e32 v47, 16, v18
	v_and_b32_e32 v18, 0xffff0000, v18
	v_lshlrev_b32_e32 v49, 16, v20
	v_and_b32_e32 v20, 0xffff0000, v20
	v_lshlrev_b32_e32 v51, 16, v22
	v_and_b32_e32 v22, 0xffff0000, v22
	v_mul_f32_e32 v45, 0x41000000, v45
	v_mul_f32_e32 v16, 0x41000000, v16
	v_mul_f32_e32 v47, 0x41000000, v47
	v_mul_f32_e32 v18, 0x41000000, v18
	v_mul_f32_e32 v49, 0x41000000, v49
	v_mul_f32_e32 v20, 0x41000000, v20
	v_mul_f32_e32 v51, 0x41000000, v51
	v_mul_f32_e32 v22, 0x41000000, v22
	v_cvt_pk_fp8_f32 v15, v45, v16
	v_cvt_pk_fp8_f32 v42, v47, v18
	v_cvt_pk_fp8_f32 v43, v49, v20
	v_cvt_pk_fp8_f32 v44, v51, v22
	v_lshlrev_b32_e32 v46, 16, v17
	v_and_b32_e32 v17, 0xffff0000, v17
	v_lshlrev_b32_e32 v48, 16, v19
	v_and_b32_e32 v19, 0xffff0000, v19
	v_lshlrev_b32_e32 v50, 16, v21
	v_and_b32_e32 v21, 0xffff0000, v21
	v_lshlrev_b32_e32 v52, 16, v23
	v_and_b32_e32 v23, 0xffff0000, v23
	v_mul_f32_e32 v46, 0x41000000, v46
	v_mul_f32_e32 v17, 0x41000000, v17
	v_mul_f32_e32 v48, 0x41000000, v48
	v_mul_f32_e32 v19, 0x41000000, v19
	v_mul_f32_e32 v50, 0x41000000, v50
	v_mul_f32_e32 v21, 0x41000000, v21
	v_mul_f32_e32 v52, 0x41000000, v52
	v_mul_f32_e32 v23, 0x41000000, v23
	v_cvt_pk_fp8_f32 v15, v46, v17 op_sel:[0,0,1]
	v_cvt_pk_fp8_f32 v42, v48, v19 op_sel:[0,0,1]
	v_cvt_pk_fp8_f32 v43, v50, v21 op_sel:[0,0,1]
	v_cvt_pk_fp8_f32 v44, v52, v23 op_sel:[0,0,1]
	v_and_b32_e32 v20, -4, v210
	v_cmp_gt_u32_e32 vcc, 4, v210
	s_nop 1
	v_cndmask_b32_e32 v75, 0, v42, vcc
	v_cndmask_b32_e32 v74, 0, v15, vcc
	v_cndmask_b32_e32 v83, 0, v44, vcc
	v_cndmask_b32_e32 v82, 0, v43, vcc
	v_cmp_eq_u32_e32 vcc, 4, v20
	s_nop 1
	v_cndmask_b32_e32 v77, 0, v42, vcc
	v_cndmask_b32_e32 v76, 0, v15, vcc
	v_cndmask_b32_e32 v119, 0, v44, vcc
	v_cndmask_b32_e32 v118, 0, v43, vcc
	s_nop 1
	s_waitcnt vmcnt(14)
	v_mfma_f32_16x16x32_fp8_fp8 v[30:33], v[156:157], v[74:75], 0
	v_mfma_f32_16x16x32_fp8_fp8 v[30:33], v[158:159], v[82:83], v[30:33]
	v_mfma_f32_16x16x32_fp8_fp8 v[30:33], v[160:161], v[76:77], v[30:33]
	v_mfma_f32_16x16x32_fp8_fp8 v[30:33], v[162:163], v[118:119], v[30:33]
	v_lshl_add_u32 v244, v56, 7, v24
	global_load_dwordx4 v[156:159], v244, s[46:47]
	global_load_dwordx4 v[160:163], v244, s[46:47] offset:64
	s_waitcnt vmcnt(14)
	v_mfma_f32_16x16x32_fp8_fp8 v[42:45], v[164:165], v[74:75], 0
	v_mfma_f32_16x16x32_fp8_fp8 v[42:45], v[166:167], v[82:83], v[42:45]
	v_mfma_f32_16x16x32_fp8_fp8 v[42:45], v[168:169], v[76:77], v[42:45]
	v_mfma_f32_16x16x32_fp8_fp8 v[42:45], v[170:171], v[118:119], v[42:45]
	v_lshl_add_u32 v244, v14, 7, v24
	global_load_dwordx4 v[164:167], v244, s[46:47]
	global_load_dwordx4 v[168:171], v244, s[46:47] offset:64
	s_waitcnt vmcnt(14)
	v_mfma_f32_16x16x32_fp8_fp8 v[46:49], v[172:173], v[74:75], 0
	v_mfma_f32_16x16x32_fp8_fp8 v[46:49], v[174:175], v[82:83], v[46:49]
	v_mfma_f32_16x16x32_fp8_fp8 v[46:49], v[176:177], v[76:77], v[46:49]
	v_mfma_f32_16x16x32_fp8_fp8 v[46:49], v[178:179], v[118:119], v[46:49]
	v_lshl_add_u32 v244, v13, 7, v24
	global_load_dwordx4 v[172:175], v244, s[46:47]
	global_load_dwordx4 v[176:179], v244, s[46:47] offset:64
	s_waitcnt vmcnt(14)
	v_mfma_f32_16x16x32_fp8_fp8 v[50:53], v[180:181], v[74:75], 0
	v_mfma_f32_16x16x32_fp8_fp8 v[50:53], v[182:183], v[82:83], v[50:53]
	v_mfma_f32_16x16x32_fp8_fp8 v[50:53], v[184:185], v[76:77], v[50:53]
	v_mfma_f32_16x16x32_fp8_fp8 v[50:53], v[186:187], v[118:119], v[50:53]
	v_lshl_add_u32 v244, v12, 7, v24
	global_load_dwordx4 v[180:183], v244, s[46:47]
	global_load_dwordx4 v[184:187], v244, s[46:47] offset:64
	s_waitcnt vmcnt(14)
	v_mfma_f32_16x16x32_fp8_fp8 v[58:61], v[188:189], v[74:75], 0
	v_mfma_f32_16x16x32_fp8_fp8 v[58:61], v[190:191], v[82:83], v[58:61]
	v_mfma_f32_16x16x32_fp8_fp8 v[58:61], v[192:193], v[76:77], v[58:61]
	v_mfma_f32_16x16x32_fp8_fp8 v[58:61], v[194:195], v[118:119], v[58:61]
	v_lshl_add_u32 v244, v9, 7, v24
	global_load_dwordx4 v[188:191], v244, s[46:47]
	global_load_dwordx4 v[192:195], v244, s[46:47] offset:64
	s_waitcnt vmcnt(14)
	v_mfma_f32_16x16x32_fp8_fp8 v[62:65], v[196:197], v[74:75], 0
	v_mfma_f32_16x16x32_fp8_fp8 v[62:65], v[198:199], v[82:83], v[62:65]
	v_mfma_f32_16x16x32_fp8_fp8 v[62:65], v[224:225], v[76:77], v[62:65]
	v_mfma_f32_16x16x32_fp8_fp8 v[62:65], v[226:227], v[118:119], v[62:65]
	v_lshl_add_u32 v244, v8, 7, v24
	global_load_dwordx4 v[196:199], v244, s[46:47]
	global_load_dwordx4 v[224:227], v244, s[46:47] offset:64
	s_waitcnt vmcnt(14)
	v_mfma_f32_16x16x32_fp8_fp8 v[70:73], v[228:229], v[74:75], 0
	v_mfma_f32_16x16x32_fp8_fp8 v[70:73], v[230:231], v[82:83], v[70:73]
	v_mfma_f32_16x16x32_fp8_fp8 v[70:73], v[232:233], v[76:77], v[70:73]
	v_mfma_f32_16x16x32_fp8_fp8 v[70:73], v[234:235], v[118:119], v[70:73]
	v_lshl_add_u32 v244, v7, 7, v24
	global_load_dwordx4 v[228:231], v244, s[46:47]
	global_load_dwordx4 v[232:235], v244, s[46:47] offset:64
	s_waitcnt vmcnt(14)
	v_mfma_f32_16x16x32_fp8_fp8 v[78:81], v[236:237], v[74:75], 0
	v_mfma_f32_16x16x32_fp8_fp8 v[78:81], v[238:239], v[82:83], v[78:81]
	v_mfma_f32_16x16x32_fp8_fp8 v[78:81], v[240:241], v[76:77], v[78:81]
	v_mfma_f32_16x16x32_fp8_fp8 v[78:81], v[242:243], v[118:119], v[78:81]
	v_lshl_add_u32 v244, v6, 7, v24
	global_load_dwordx4 v[236:239], v244, s[46:47]
	global_load_dwordx4 v[240:243], v244, s[46:47] offset:64
	v_lshl_add_u32 v246, v5, 7, v116
	v_lshl_add_u32 v248, v4, 7, v116
	v_lshl_add_u32 v250, v11, 7, v116
	v_lshl_add_u32 v252, v10, 7, v116
	global_load_dwordx4 v[2:5], v246, s[48:49]
	global_load_dwordx4 v[6:9], v248, s[48:49]
	global_load_dwordx4 v[10:13], v250, s[48:49]
	global_load_dwordx4 v[14:17], v252, s[48:49]
	s_waitcnt vmcnt(18)
	v_mfma_f32_16x16x32_fp8_fp8 v[18:21], v[156:157], v[74:75], 0
	v_mfma_f32_16x16x32_fp8_fp8 v[18:21], v[158:159], v[82:83], v[18:21]
	v_mfma_f32_16x16x32_fp8_fp8 v[18:21], v[160:161], v[76:77], v[18:21]
	v_mfma_f32_16x16x32_fp8_fp8 v[18:21], v[162:163], v[118:119], v[18:21]
	s_waitcnt vmcnt(16)
	v_mfma_f32_16x16x32_fp8_fp8 v[22:25], v[164:165], v[74:75], 0
	v_mfma_f32_16x16x32_fp8_fp8 v[22:25], v[166:167], v[82:83], v[22:25]
	v_mfma_f32_16x16x32_fp8_fp8 v[22:25], v[168:169], v[76:77], v[22:25]
	v_mfma_f32_16x16x32_fp8_fp8 v[22:25], v[170:171], v[118:119], v[22:25]
	s_waitcnt vmcnt(14)
	v_mfma_f32_16x16x32_fp8_fp8 v[26:29], v[172:173], v[74:75], 0
	v_mfma_f32_16x16x32_fp8_fp8 v[26:29], v[174:175], v[82:83], v[26:29]
	v_mfma_f32_16x16x32_fp8_fp8 v[26:29], v[176:177], v[76:77], v[26:29]
	v_mfma_f32_16x16x32_fp8_fp8 v[26:29], v[178:179], v[118:119], v[26:29]
	s_waitcnt vmcnt(12)
	v_mfma_f32_16x16x32_fp8_fp8 v[34:37], v[180:181], v[74:75], 0
	v_mfma_f32_16x16x32_fp8_fp8 v[34:37], v[182:183], v[82:83], v[34:37]
	v_mfma_f32_16x16x32_fp8_fp8 v[34:37], v[184:185], v[76:77], v[34:37]
	v_mfma_f32_16x16x32_fp8_fp8 v[34:37], v[186:187], v[118:119], v[34:37]
	s_waitcnt vmcnt(10)
	v_mfma_f32_16x16x32_fp8_fp8 v[38:41], v[188:189], v[74:75], 0
	v_mfma_f32_16x16x32_fp8_fp8 v[38:41], v[190:191], v[82:83], v[38:41]
	v_mfma_f32_16x16x32_fp8_fp8 v[38:41], v[192:193], v[76:77], v[38:41]
	v_mfma_f32_16x16x32_fp8_fp8 v[38:41], v[194:195], v[118:119], v[38:41]
	s_waitcnt vmcnt(8)
	v_mfma_f32_16x16x32_fp8_fp8 v[54:57], v[196:197], v[74:75], 0
	v_mfma_f32_16x16x32_fp8_fp8 v[54:57], v[198:199], v[82:83], v[54:57]
	v_mfma_f32_16x16x32_fp8_fp8 v[54:57], v[224:225], v[76:77], v[54:57]
	v_mfma_f32_16x16x32_fp8_fp8 v[54:57], v[226:227], v[118:119], v[54:57]
	s_waitcnt vmcnt(6)
	v_mfma_f32_16x16x32_fp8_fp8 v[66:69], v[228:229], v[74:75], 0
	v_mfma_f32_16x16x32_fp8_fp8 v[66:69], v[230:231], v[82:83], v[66:69]
	v_mfma_f32_16x16x32_fp8_fp8 v[66:69], v[232:233], v[76:77], v[66:69]
	v_mfma_f32_16x16x32_fp8_fp8 v[66:69], v[234:235], v[118:119], v[66:69]
	s_waitcnt vmcnt(4)
	v_mfma_f32_16x16x32_fp8_fp8 v[248:251], v[236:237], v[74:75], 0
	v_mfma_f32_16x16x32_fp8_fp8 v[248:251], v[238:239], v[82:83], v[248:251]
	v_mfma_f32_16x16x32_fp8_fp8 v[74:77], v[240:241], v[76:77], v[248:251]
	v_mfma_f32_16x16x32_fp8_fp8 v[74:77], v[242:243], v[118:119], v[74:77]
	s_nop 7
	ds_read2_b64 v[82:85], v121 offset0:56 offset1:60
	v_lshl_add_u32 v140, v120, 2, s22
	s_waitcnt lgkmcnt(0)
	s_cmpk_lt_i32 s97, 0xff
	s_mov_b64 s[8:9], -1
	s_cbranch_scc0 .LBB0_1332
	v_cmp_ge_i32_e32 vcc, s10, v117
	v_mov_b32_e32 v119, 0xff800000
	v_mov_b32_e32 v118, 0xff800000
	s_and_saveexec_b64 s[8:9], vcc
	s_cbranch_execz .LBB0_1205
	s_waitcnt lgkmcnt(7)
	v_sub_u32_sdwa v118, s97, v110 dst_sel:DWORD dst_unused:UNUSED_PAD src0_sel:DWORD src1_sel:WORD_0
	v_min_i32_e32 v118, 0x71, v118
	v_lshl_add_u32 v118, v118, 5, v140
	ds_read_b32 v118, v118
	s_waitcnt lgkmcnt(0)
	v_fmac_f32_e32 v118, 0x3e000000, v30

.LBB0_1334:
	v_and_b32_e32 v34, 64, v209
	v_max_f32_e32 v21, v215, v215
	v_mov_b32_e32 v32, v141
	v_mov_b32_e32 v33, v141
	v_max_f32_e32 v20, v215, v215
	v_readlane_b32 s9, v254, 54
	s_movk_i32 s8, 0x520
	v_lshlrev_b32_e32 v34, 2, v34
	v_permlane16_swap_b32_e32 v20, v21
	s_lshl_b64 s[0:1], s[0:1], 9
	s_lshl_b64 s[0:1], s[0:1], 1
	v_max_f32_e32 v20, v20, v21
	v_mov_b32_e32 v21, v20
	s_nop 1
	v_permlane32_swap_b32_e32 v20, v21
	s_nop 1
	v_max_f32_e32 v20, v20, v21
	v_add_f32_e32 v20, 0xc1000000, v20
	v_pk_add_f32 v[118:119], v[118:119], v[20:21] op_sel_hi:[1,0] neg_lo:[0,1] neg_hi:[0,1]
	v_pk_add_f32 v[120:121], v[120:121], v[20:21] op_sel_hi:[1,0] neg_lo:[0,1] neg_hi:[0,1]
	v_pk_add_f32 v[122:123], v[122:123], v[20:21] op_sel_hi:[1,0] neg_lo:[0,1] neg_hi:[0,1]
	v_pk_add_f32 v[124:125], v[124:125], v[20:21] op_sel_hi:[1,0] neg_lo:[0,1] neg_hi:[0,1]
	v_pk_add_f32 v[126:127], v[126:127], v[20:21] op_sel_hi:[1,0] neg_lo:[0,1] neg_hi:[0,1]
	v_pk_add_f32 v[128:129], v[128:129], v[20:21] op_sel_hi:[1,0] neg_lo:[0,1] neg_hi:[0,1]
	v_pk_add_f32 v[130:131], v[130:131], v[20:21] op_sel_hi:[1,0] neg_lo:[0,1] neg_hi:[0,1]
	v_pk_add_f32 v[132:133], v[132:133], v[20:21] op_sel_hi:[1,0] neg_lo:[0,1] neg_hi:[0,1]
	v_pk_add_f32 v[134:135], v[134:135], v[20:21] op_sel_hi:[1,0] neg_lo:[0,1] neg_hi:[0,1]
	v_pk_add_f32 v[136:137], v[136:137], v[20:21] op_sel_hi:[1,0] neg_lo:[0,1] neg_hi:[0,1]
	v_pk_add_f32 v[156:157], v[156:157], v[20:21] op_sel_hi:[1,0] neg_lo:[0,1] neg_hi:[0,1]
	v_pk_add_f32 v[158:159], v[158:159], v[20:21] op_sel_hi:[1,0] neg_lo:[0,1] neg_hi:[0,1]
	v_pk_add_f32 v[160:161], v[160:161], v[20:21] op_sel_hi:[1,0] neg_lo:[0,1] neg_hi:[0,1]
	v_pk_add_f32 v[162:163], v[162:163], v[20:21] op_sel_hi:[1,0] neg_lo:[0,1] neg_hi:[0,1]
	v_pk_add_f32 v[164:165], v[164:165], v[20:21] op_sel_hi:[1,0] neg_lo:[0,1] neg_hi:[0,1]
	v_pk_add_f32 v[166:167], v[166:167], v[20:21] op_sel_hi:[1,0] neg_lo:[0,1] neg_hi:[0,1]
	v_pk_add_f32 v[168:169], v[168:169], v[20:21] op_sel_hi:[1,0] neg_lo:[0,1] neg_hi:[0,1]
	v_pk_add_f32 v[170:171], v[170:171], v[20:21] op_sel_hi:[1,0] neg_lo:[0,1] neg_hi:[0,1]
	v_pk_add_f32 v[172:173], v[172:173], v[20:21] op_sel_hi:[1,0] neg_lo:[0,1] neg_hi:[0,1]
	v_pk_add_f32 v[174:175], v[174:175], v[20:21] op_sel_hi:[1,0] neg_lo:[0,1] neg_hi:[0,1]
	v_pk_add_f32 v[176:177], v[176:177], v[20:21] op_sel_hi:[1,0] neg_lo:[0,1] neg_hi:[0,1]
	v_pk_add_f32 v[178:179], v[178:179], v[20:21] op_sel_hi:[1,0] neg_lo:[0,1] neg_hi:[0,1]
	v_pk_add_f32 v[180:181], v[180:181], v[20:21] op_sel_hi:[1,0] neg_lo:[0,1] neg_hi:[0,1]
	v_pk_add_f32 v[182:183], v[182:183], v[20:21] op_sel_hi:[1,0] neg_lo:[0,1] neg_hi:[0,1]
	v_pk_add_f32 v[184:185], v[184:185], v[20:21] op_sel_hi:[1,0] neg_lo:[0,1] neg_hi:[0,1]
	v_pk_add_f32 v[186:187], v[186:187], v[20:21] op_sel_hi:[1,0] neg_lo:[0,1] neg_hi:[0,1]
	v_pk_add_f32 v[188:189], v[188:189], v[20:21] op_sel_hi:[1,0] neg_lo:[0,1] neg_hi:[0,1]
	v_pk_add_f32 v[190:191], v[190:191], v[20:21] op_sel_hi:[1,0] neg_lo:[0,1] neg_hi:[0,1]
	v_pk_add_f32 v[192:193], v[192:193], v[20:21] op_sel_hi:[1,0] neg_lo:[0,1] neg_hi:[0,1]
	v_pk_add_f32 v[194:195], v[194:195], v[20:21] op_sel_hi:[1,0] neg_lo:[0,1] neg_hi:[0,1]
	v_pk_add_f32 v[196:197], v[196:197], v[20:21] op_sel_hi:[1,0] neg_lo:[0,1] neg_hi:[0,1]
	v_pk_add_f32 v[198:199], v[198:199], v[20:21] op_sel_hi:[1,0] neg_lo:[0,1] neg_hi:[0,1]
	v_exp_f32_e32 v21, v118
	v_exp_f32_e32 v23, v119
	v_exp_f32_e32 v24, v120
	v_exp_f32_e32 v25, v121
	v_exp_f32_e32 v26, v122
	v_exp_f32_e32 v27, v123
	v_exp_f32_e32 v28, v124
	v_exp_f32_e32 v29, v125
	v_exp_f32_e32 v31, v126
	v_exp_f32_e32 v36, v127
	v_exp_f32_e32 v37, v128
	v_exp_f32_e32 v38, v129
	v_exp_f32_e32 v39, v130
	v_exp_f32_e32 v40, v131
	v_exp_f32_e32 v41, v132
	v_exp_f32_e32 v42, v133
	v_exp_f32_e32 v43, v134
	v_exp_f32_e32 v44, v135
	v_exp_f32_e32 v45, v136
	v_exp_f32_e32 v46, v137
	v_exp_f32_e32 v47, v156
	v_exp_f32_e32 v48, v157
	v_exp_f32_e32 v49, v158
	v_exp_f32_e32 v50, v159
	v_exp_f32_e32 v51, v160
	v_exp_f32_e32 v52, v161
	v_exp_f32_e32 v53, v162
	v_exp_f32_e32 v54, v163
	v_exp_f32_e32 v55, v164
	v_exp_f32_e32 v56, v165
	v_exp_f32_e32 v57, v166
	v_exp_f32_e32 v58, v167
	v_exp_f32_e32 v59, v168
	v_exp_f32_e32 v60, v169
	v_exp_f32_e32 v61, v170
	v_exp_f32_e32 v62, v171
	v_exp_f32_e32 v63, v172
	v_exp_f32_e32 v64, v173
	v_exp_f32_e32 v65, v174
	v_exp_f32_e32 v66, v175
	v_exp_f32_e32 v67, v176
	v_exp_f32_e32 v68, v177
	v_exp_f32_e32 v69, v178
	v_exp_f32_e32 v70, v179
	v_exp_f32_e32 v71, v180
	v_exp_f32_e32 v72, v181
	v_exp_f32_e32 v73, v182
	v_exp_f32_e32 v74, v183
	v_exp_f32_e32 v75, v184
	v_exp_f32_e32 v76, v185
	v_exp_f32_e32 v77, v186
	v_exp_f32_e32 v78, v187
	v_exp_f32_e32 v79, v188
	v_exp_f32_e32 v80, v189
	v_exp_f32_e32 v81, v190
	v_exp_f32_e32 v82, v191
	v_exp_f32_e32 v83, v192
	v_exp_f32_e32 v84, v193
	v_exp_f32_e32 v85, v194
	v_exp_f32_e32 v86, v195
	v_exp_f32_e32 v87, v196
	v_exp_f32_e32 v88, v197
	v_exp_f32_e32 v89, v198
	v_exp_f32_e32 v90, v199
	s_nop 0
	v_pk_add_f32 v[118:119], v[24:25], v[38:39]
	v_pk_add_f32 v[120:121], v[26:27], v[40:41]
	v_pk_add_f32 v[122:123], v[28:29], v[42:43]
	v_pk_add_f32 v[124:125], v[36:37], v[44:45]
	v_pk_add_f32 v[118:119], v[118:119], v[46:47]
	v_pk_add_f32 v[120:121], v[120:121], v[48:49]
	v_pk_add_f32 v[122:123], v[122:123], v[50:51]
	v_pk_add_f32 v[124:125], v[124:125], v[52:53]
	v_pk_add_f32 v[118:119], v[118:119], v[54:55]
	v_pk_add_f32 v[120:121], v[120:121], v[56:57]
	v_pk_add_f32 v[122:123], v[122:123], v[58:59]
	v_pk_add_f32 v[124:125], v[124:125], v[60:61]
	v_pk_add_f32 v[118:119], v[118:119], v[62:63]
	v_pk_add_f32 v[120:121], v[120:121], v[64:65]
	v_pk_add_f32 v[122:123], v[122:123], v[66:67]
	v_pk_add_f32 v[124:125], v[124:125], v[68:69]
	v_pk_add_f32 v[118:119], v[118:119], v[70:71]
	v_pk_add_f32 v[120:121], v[120:121], v[72:73]
	v_pk_add_f32 v[122:123], v[122:123], v[74:75]
	v_pk_add_f32 v[124:125], v[124:125], v[76:77]
	v_pk_add_f32 v[118:119], v[118:119], v[78:79]
	v_pk_add_f32 v[120:121], v[120:121], v[80:81]
	v_pk_add_f32 v[122:123], v[122:123], v[82:83]
	v_pk_add_f32 v[124:125], v[124:125], v[84:85]
	v_pk_add_f32 v[118:119], v[118:119], v[86:87]
	v_pk_add_f32 v[120:121], v[120:121], v[88:89]
	v_pk_add_f32 v[118:119], v[118:119], v[120:121]
	v_pk_add_f32 v[122:123], v[122:123], v[124:125]
	v_add_f32_e32 v126, v21, v23
	v_add_f32_e32 v127, v31, v90
	v_pk_add_f32 v[118:119], v[118:119], v[122:123]
	v_add_f32_e32 v126, v126, v127
	v_add_f32_e32 v20, v118, v119
	v_add_f32_e32 v20, v20, v126
	v_mov_b32_e32 v18, v20
	v_cvt_pk_fp8_f32 v32, v21, v23
	v_cvt_pk_fp8_f32 v33, v26, v27
	v_permlane16_swap_b32_e32 v18, v20
	v_mov_b32_e32 v30, v141
	v_cvt_pk_fp8_f32 v30, v31, v36
	v_add_f32_e32 v18, v20, v18
	v_mov_b32_e32 v19, v18
	v_cvt_pk_fp8_f32 v32, v24, v25 op_sel:[0,0,1]
	v_cvt_pk_fp8_f32 v33, v28, v29 op_sel:[0,0,1]
	v_permlane32_swap_b32_e32 v18, v19
	v_mov_b32_e32 v31, v141
	v_mov_b32_e32 v28, v141
	v_add_f32_e32 v35, v18, v19
	v_mov_b32_e32 v29, v141
	v_mov_b32_e32 v24, v141
	v_mov_b32_e32 v25, v141
	v_mov_b32_e32 v22, v141
	v_mov_b32_e32 v23, v141
	v_mov_b32_e32 v20, v141
	v_mov_b32_e32 v21, v141
	v_mov_b32_e32 v18, v141
	v_mov_b32_e32 v19, v141
	v_mov_b32_e32 v26, v141
	v_mov_b32_e32 v27, v141
	v_cvt_pk_fp8_f32 v31, v39, v40
	v_cvt_pk_fp8_f32 v28, v43, v44
	v_cvt_pk_fp8_f32 v29, v47, v48
	v_cvt_pk_fp8_f32 v24, v51, v52
	v_cvt_pk_fp8_f32 v25, v55, v56
	v_cvt_pk_fp8_f32 v22, v59, v60
	v_cvt_pk_fp8_f32 v23, v63, v64
	v_cvt_pk_fp8_f32 v20, v67, v68
	v_cvt_pk_fp8_f32 v21, v71, v72
	v_cvt_pk_fp8_f32 v18, v75, v76
	v_cvt_pk_fp8_f32 v19, v79, v80
	v_cvt_pk_fp8_f32 v26, v83, v84
	v_cvt_pk_fp8_f32 v27, v87, v88
	v_cvt_pk_fp8_f32 v30, v37, v38 op_sel:[0,0,1]
	v_cvt_pk_fp8_f32 v31, v41, v42 op_sel:[0,0,1]
	v_cvt_pk_fp8_f32 v28, v45, v46 op_sel:[0,0,1]
	v_cvt_pk_fp8_f32 v29, v49, v50 op_sel:[0,0,1]
	v_cvt_pk_fp8_f32 v24, v53, v54 op_sel:[0,0,1]
	v_cvt_pk_fp8_f32 v25, v57, v58 op_sel:[0,0,1]
	v_cvt_pk_fp8_f32 v22, v61, v62 op_sel:[0,0,1]
	v_cvt_pk_fp8_f32 v23, v65, v66 op_sel:[0,0,1]
	v_cvt_pk_fp8_f32 v20, v69, v70 op_sel:[0,0,1]
	v_cvt_pk_fp8_f32 v21, v73, v74 op_sel:[0,0,1]
	v_cvt_pk_fp8_f32 v18, v77, v78 op_sel:[0,0,1]
	v_cvt_pk_fp8_f32 v19, v81, v82 op_sel:[0,0,1]
	v_cvt_pk_fp8_f32 v26, v85, v86 op_sel:[0,0,1]
	v_cvt_pk_fp8_f32 v27, v89, v90 op_sel:[0,0,1]
	s_nop 0
	ds_read_u16 v86, v212 offset:64
	ds_read_u16 v87, v212 offset:80
	ds_read_u16 v88, v212 offset:96
	ds_read_u16 v89, v212 offset:112
	ds_read_u16 v90, v212 offset:128
	ds_read_u16 v91, v212 offset:144
	ds_read_u16 v92, v212 offset:160
	ds_read_u16 v93, v212 offset:176
	ds_read_u16 v94, v212 offset:192
	ds_read_u16 v95, v212 offset:208
	ds_read_u16 v96, v212 offset:224
	ds_read_u16 v97, v212 offset:240
	ds_read_u16 v98, v212 offset:256
	ds_read_u16 v99, v212 offset:272
	ds_read_u16 v100, v212 offset:288
	ds_read_u16 v101, v212 offset:304
	ds_read_u16 v102, v212 offset:320
	ds_read_u16 v103, v212 offset:336
	ds_read_u16 v104, v212 offset:352
	ds_read_u16 v105, v212 offset:368
	ds_read_u16 v106, v212 offset:384
	ds_read_u16 v107, v212 offset:400
	ds_read_u16 v108, v212 offset:416
	ds_read_u16 v109, v212 offset:432
	ds_read_u16 v110, v212 offset:448
	ds_read_u16 v111, v212 offset:464
	ds_read_u16 v112, v212 offset:480
	ds_read_u16 v113, v212 offset:496
	v_ashrrev_i32_e32 v36, 1, v210
	v_cmp_gt_i32_e32 vcc, 4, v36
	v_add_u32_e32 v37, 12, v117
	v_mov_b32_e32 v54, s9
	v_cndmask_b32_e32 v37, v37, v117, vcc
	v_add_u32_e32 v36, v37, v36
	v_and_b32_e32 v37, 15, v36
	v_mad_u32_u24 v37, v37, s24, v54
	v_lshrrev_b32_e32 v36, 4, v36
	v_lshlrev_b32_e32 v54, 3, v210
	v_mul_lo_u32 v36, v36, s8
	v_and_b32_e32 v54, 8, v54
	v_add3_u32 v36, v37, v36, v54
	v_lshrrev_b32_e32 v37, 2, v214
	s_movk_i32 s8, 0xa40
	v_mul_lo_u32 v37, v37, s8
	v_add_u32_e32 v37, s9, v37
	v_and_b32_e32 v54, 48, v116
	v_mul_lo_u32 v55, v213, s24
	v_add3_u32 v37, v37, v54, v55
	s_waitcnt lgkmcnt(0)
	v_lshl_add_u32 v244, v86, 7, v116
	global_load_dwordx4 v[38:41], v244, s[48:49]
	v_lshl_add_u32 v246, v87, 7, v116
	global_load_dwordx4 v[42:45], v246, s[48:49]
	v_lshl_add_u32 v248, v88, 7, v116
	global_load_dwordx4 v[46:49], v248, s[48:49]
	v_lshl_add_u32 v250, v89, 7, v116
	global_load_dwordx4 v[50:53], v250, s[48:49]
	v_lshl_add_u32 v244, v90, 7, v116
	global_load_dwordx4 v[156:159], v244, s[48:49]
	v_lshl_add_u32 v246, v91, 7, v116
	global_load_dwordx4 v[160:163], v246, s[48:49]
	v_lshl_add_u32 v248, v92, 7, v116
	global_load_dwordx4 v[164:167], v248, s[48:49]
	v_lshl_add_u32 v250, v93, 7, v116
	global_load_dwordx4 v[168:171], v250, s[48:49]
	v_lshl_add_u32 v244, v94, 7, v116
	global_load_dwordx4 v[172:175], v244, s[48:49]
	v_lshl_add_u32 v246, v95, 7, v116
	global_load_dwordx4 v[176:179], v246, s[48:49]
	v_lshl_add_u32 v248, v96, 7, v116
	global_load_dwordx4 v[180:183], v248, s[48:49]
	v_lshl_add_u32 v250, v97, 7, v116
	global_load_dwordx4 v[184:187], v250, s[48:49]
	v_lshl_add_u32 v244, v98, 7, v116
	global_load_dwordx4 v[188:191], v244, s[48:49]
	v_lshl_add_u32 v246, v99, 7, v116
	global_load_dwordx4 v[192:195], v246, s[48:49]
	v_lshl_add_u32 v248, v100, 7, v116
	global_load_dwordx4 v[196:199], v248, s[48:49]
	v_lshl_add_u32 v250, v101, 7, v116
	global_load_dwordx4 v[224:227], v250, s[48:49]
	v_lshl_add_u32 v244, v102, 7, v116
	global_load_dwordx4 v[228:231], v244, s[48:49]
	v_lshl_add_u32 v246, v103, 7, v116
	global_load_dwordx4 v[232:235], v246, s[48:49]
	v_lshl_add_u32 v248, v104, 7, v116
	global_load_dwordx4 v[236:239], v248, s[48:49]
	v_lshl_add_u32 v250, v105, 7, v116
	global_load_dwordx4 v[240:243], v250, s[48:49]
	s_waitcnt vmcnt(23)
	ds_write_b128 v37, v[2:5]
	s_waitcnt vmcnt(22)
	ds_write_b128 v37, v[6:9] offset:640
	s_waitcnt vmcnt(21)
	ds_write_b128 v37, v[10:13] offset:1312
	s_waitcnt vmcnt(20)
	ds_write_b128 v37, v[14:17] offset:1952
	v_lshl_add_u32 v244, v106, 7, v116
	global_load_dwordx4 v[2:5], v244, s[48:49]
	v_lshl_add_u32 v246, v107, 7, v116
	global_load_dwordx4 v[6:9], v246, s[48:49]
	v_lshl_add_u32 v248, v108, 7, v116
	global_load_dwordx4 v[10:13], v248, s[48:49]
	v_lshl_add_u32 v250, v109, 7, v116
	global_load_dwordx4 v[14:17], v250, s[48:49]
	s_waitcnt lgkmcnt(0)
	ds_read_b64_tr_b8 v[86:87], v36 offset:0
	ds_read_b64_tr_b8 v[88:89], v36 offset:16
	ds_read_b64_tr_b8 v[90:91], v36 offset:32
	ds_read_b64_tr_b8 v[92:93], v36 offset:48
	ds_read_b64_tr_b8 v[94:95], v36 offset:2624
	ds_read_b64_tr_b8 v[96:97], v36 offset:2640
	ds_read_b64_tr_b8 v[98:99], v36 offset:2656
	ds_read_b64_tr_b8 v[100:101], v36 offset:2672
	s_waitcnt lgkmcnt(0)
	s_waitcnt vmcnt(23)
	ds_write_b128 v37, v[38:41]
	s_waitcnt vmcnt(22)
	ds_write_b128 v37, v[42:45] offset:640
	s_waitcnt vmcnt(21)
	ds_write_b128 v37, v[46:49] offset:1312
	s_waitcnt vmcnt(20)
	ds_write_b128 v37, v[50:53] offset:1952
	v_lshl_add_u32 v244, v110, 7, v116
	global_load_dwordx4 v[38:41], v244, s[48:49]
	v_lshl_add_u32 v246, v111, 7, v116
	global_load_dwordx4 v[42:45], v246, s[48:49]
	v_lshl_add_u32 v248, v112, 7, v116
	global_load_dwordx4 v[46:49], v248, s[48:49]
	v_lshl_add_u32 v250, v113, 7, v116
	global_load_dwordx4 v[50:53], v250, s[48:49]
	v_mfma_f32_16x16x32_fp8_fp8 v[54:57], v[32:33], v[86:87], 0
	v_mfma_f32_16x16x32_fp8_fp8 v[58:61], v[32:33], v[88:89], 0
	v_mfma_f32_16x16x32_fp8_fp8 v[62:65], v[32:33], v[90:91], 0
	v_mfma_f32_16x16x32_fp8_fp8 v[66:69], v[32:33], v[92:93], 0
	v_mfma_f32_16x16x32_fp8_fp8 v[70:73], v[32:33], v[94:95], 0
	v_mfma_f32_16x16x32_fp8_fp8 v[74:77], v[32:33], v[96:97], 0
	v_mfma_f32_16x16x32_fp8_fp8 v[78:81], v[32:33], v[98:99], 0
	v_mfma_f32_16x16x32_fp8_fp8 v[82:85], v[32:33], v[100:101], 0
	s_waitcnt lgkmcnt(0)
	ds_read_b64_tr_b8 v[86:87], v36 offset:0
	ds_read_b64_tr_b8 v[88:89], v36 offset:16
	ds_read_b64_tr_b8 v[90:91], v36 offset:32
	ds_read_b64_tr_b8 v[92:93], v36 offset:48
	ds_read_b64_tr_b8 v[94:95], v36 offset:2624
	ds_read_b64_tr_b8 v[96:97], v36 offset:2640
	ds_read_b64_tr_b8 v[98:99], v36 offset:2656
	ds_read_b64_tr_b8 v[100:101], v36 offset:2672
	s_waitcnt lgkmcnt(0)
	s_waitcnt vmcnt(23)
	ds_write_b128 v37, v[156:159]
	s_waitcnt vmcnt(22)
	ds_write_b128 v37, v[160:163] offset:640
	s_waitcnt vmcnt(21)
	ds_write_b128 v37, v[164:167] offset:1312
	s_waitcnt vmcnt(20)
	ds_write_b128 v37, v[168:171] offset:1952
	v_mfma_f32_16x16x32_fp8_fp8 v[54:57], v[30:31], v[86:87], v[54:57]
	v_mfma_f32_16x16x32_fp8_fp8 v[58:61], v[30:31], v[88:89], v[58:61]
	v_mfma_f32_16x16x32_fp8_fp8 v[62:65], v[30:31], v[90:91], v[62:65]
	v_mfma_f32_16x16x32_fp8_fp8 v[66:69], v[30:31], v[92:93], v[66:69]
	v_mfma_f32_16x16x32_fp8_fp8 v[70:73], v[30:31], v[94:95], v[70:73]
	v_mfma_f32_16x16x32_fp8_fp8 v[74:77], v[30:31], v[96:97], v[74:77]
	v_mfma_f32_16x16x32_fp8_fp8 v[78:81], v[30:31], v[98:99], v[78:81]
	v_mfma_f32_16x16x32_fp8_fp8 v[82:85], v[30:31], v[100:101], v[82:85]
	s_waitcnt lgkmcnt(0)
	ds_read_b64_tr_b8 v[86:87], v36 offset:0
	ds_read_b64_tr_b8 v[88:89], v36 offset:16
	ds_read_b64_tr_b8 v[90:91], v36 offset:32
	ds_read_b64_tr_b8 v[92:93], v36 offset:48
	ds_read_b64_tr_b8 v[94:95], v36 offset:2624
	ds_read_b64_tr_b8 v[96:97], v36 offset:2640
	ds_read_b64_tr_b8 v[98:99], v36 offset:2656
	ds_read_b64_tr_b8 v[100:101], v36 offset:2672
	s_waitcnt lgkmcnt(0)
	s_waitcnt vmcnt(19)
	ds_write_b128 v37, v[172:175]
	s_waitcnt vmcnt(18)
	ds_write_b128 v37, v[176:179] offset:640
	s_waitcnt vmcnt(17)
	ds_write_b128 v37, v[180:183] offset:1312
	s_waitcnt vmcnt(16)
	ds_write_b128 v37, v[184:187] offset:1952
	v_mfma_f32_16x16x32_fp8_fp8 v[54:57], v[28:29], v[86:87], v[54:57]
	v_mfma_f32_16x16x32_fp8_fp8 v[58:61], v[28:29], v[88:89], v[58:61]
	v_mfma_f32_16x16x32_fp8_fp8 v[62:65], v[28:29], v[90:91], v[62:65]
	v_mfma_f32_16x16x32_fp8_fp8 v[66:69], v[28:29], v[92:93], v[66:69]
	v_mfma_f32_16x16x32_fp8_fp8 v[70:73], v[28:29], v[94:95], v[70:73]
	v_mfma_f32_16x16x32_fp8_fp8 v[74:77], v[28:29], v[96:97], v[74:77]
	v_mfma_f32_16x16x32_fp8_fp8 v[78:81], v[28:29], v[98:99], v[78:81]
	v_mfma_f32_16x16x32_fp8_fp8 v[82:85], v[28:29], v[100:101], v[82:85]
	s_waitcnt lgkmcnt(0)
	ds_read_b64_tr_b8 v[86:87], v36 offset:0
	ds_read_b64_tr_b8 v[88:89], v36 offset:16
	ds_read_b64_tr_b8 v[90:91], v36 offset:32
	ds_read_b64_tr_b8 v[92:93], v36 offset:48
	ds_read_b64_tr_b8 v[94:95], v36 offset:2624
	ds_read_b64_tr_b8 v[96:97], v36 offset:2640
	ds_read_b64_tr_b8 v[98:99], v36 offset:2656
	ds_read_b64_tr_b8 v[100:101], v36 offset:2672
	s_waitcnt lgkmcnt(0)
	s_waitcnt vmcnt(15)
	ds_write_b128 v37, v[188:191]
	s_waitcnt vmcnt(14)
	ds_write_b128 v37, v[192:195] offset:640
	s_waitcnt vmcnt(13)
	ds_write_b128 v37, v[196:199] offset:1312
	s_waitcnt vmcnt(12)
	ds_write_b128 v37, v[224:227] offset:1952
	v_mfma_f32_16x16x32_fp8_fp8 v[54:57], v[24:25], v[86:87], v[54:57]
	v_mfma_f32_16x16x32_fp8_fp8 v[58:61], v[24:25], v[88:89], v[58:61]
	v_mfma_f32_16x16x32_fp8_fp8 v[62:65], v[24:25], v[90:91], v[62:65]
	v_mfma_f32_16x16x32_fp8_fp8 v[66:69], v[24:25], v[92:93], v[66:69]
	v_mfma_f32_16x16x32_fp8_fp8 v[70:73], v[24:25], v[94:95], v[70:73]
	v_mfma_f32_16x16x32_fp8_fp8 v[74:77], v[24:25], v[96:97], v[74:77]
	v_mfma_f32_16x16x32_fp8_fp8 v[78:81], v[24:25], v[98:99], v[78:81]
	v_mfma_f32_16x16x32_fp8_fp8 v[82:85], v[24:25], v[100:101], v[82:85]
	s_waitcnt lgkmcnt(0)
	ds_read_b64_tr_b8 v[86:87], v36 offset:0
	ds_read_b64_tr_b8 v[88:89], v36 offset:16
	ds_read_b64_tr_b8 v[90:91], v36 offset:32
	ds_read_b64_tr_b8 v[92:93], v36 offset:48
	ds_read_b64_tr_b8 v[94:95], v36 offset:2624
	ds_read_b64_tr_b8 v[96:97], v36 offset:2640
	ds_read_b64_tr_b8 v[98:99], v36 offset:2656
	ds_read_b64_tr_b8 v[100:101], v36 offset:2672
	s_waitcnt lgkmcnt(0)
	s_waitcnt vmcnt(11)
	ds_write_b128 v37, v[228:231]
	s_waitcnt vmcnt(10)
	ds_write_b128 v37, v[232:235] offset:640
	s_waitcnt vmcnt(9)
	ds_write_b128 v37, v[236:239] offset:1312
	s_waitcnt vmcnt(8)
	ds_write_b128 v37, v[240:243] offset:1952
	v_mfma_f32_16x16x32_fp8_fp8 v[54:57], v[22:23], v[86:87], v[54:57]
	v_mfma_f32_16x16x32_fp8_fp8 v[58:61], v[22:23], v[88:89], v[58:61]
	v_mfma_f32_16x16x32_fp8_fp8 v[62:65], v[22:23], v[90:91], v[62:65]
	v_mfma_f32_16x16x32_fp8_fp8 v[66:69], v[22:23], v[92:93], v[66:69]
	v_mfma_f32_16x16x32_fp8_fp8 v[70:73], v[22:23], v[94:95], v[70:73]
	v_mfma_f32_16x16x32_fp8_fp8 v[74:77], v[22:23], v[96:97], v[74:77]
	v_mfma_f32_16x16x32_fp8_fp8 v[78:81], v[22:23], v[98:99], v[78:81]
	v_mfma_f32_16x16x32_fp8_fp8 v[82:85], v[22:23], v[100:101], v[82:85]
	s_waitcnt lgkmcnt(0)
	ds_read_b64_tr_b8 v[86:87], v36 offset:0
	ds_read_b64_tr_b8 v[88:89], v36 offset:16
	ds_read_b64_tr_b8 v[90:91], v36 offset:32
	ds_read_b64_tr_b8 v[92:93], v36 offset:48
	ds_read_b64_tr_b8 v[94:95], v36 offset:2624
	ds_read_b64_tr_b8 v[96:97], v36 offset:2640
	ds_read_b64_tr_b8 v[98:99], v36 offset:2656
	ds_read_b64_tr_b8 v[100:101], v36 offset:2672
	s_waitcnt lgkmcnt(0)
	s_waitcnt vmcnt(7)
	ds_write_b128 v37, v[2:5]
	s_waitcnt vmcnt(6)
	ds_write_b128 v37, v[6:9] offset:640
	s_waitcnt vmcnt(5)
	ds_write_b128 v37, v[10:13] offset:1312
	s_waitcnt vmcnt(4)
	ds_write_b128 v37, v[14:17] offset:1952
	v_mfma_f32_16x16x32_fp8_fp8 v[54:57], v[20:21], v[86:87], v[54:57]
	v_mfma_f32_16x16x32_fp8_fp8 v[58:61], v[20:21], v[88:89], v[58:61]
	v_mfma_f32_16x16x32_fp8_fp8 v[62:65], v[20:21], v[90:91], v[62:65]
	v_mfma_f32_16x16x32_fp8_fp8 v[66:69], v[20:21], v[92:93], v[66:69]
	v_mfma_f32_16x16x32_fp8_fp8 v[70:73], v[20:21], v[94:95], v[70:73]
	v_mfma_f32_16x16x32_fp8_fp8 v[74:77], v[20:21], v[96:97], v[74:77]
	v_mfma_f32_16x16x32_fp8_fp8 v[78:81], v[20:21], v[98:99], v[78:81]
	v_mfma_f32_16x16x32_fp8_fp8 v[82:85], v[20:21], v[100:101], v[82:85]
	s_waitcnt lgkmcnt(0)
	ds_read_b64_tr_b8 v[86:87], v36 offset:0
	ds_read_b64_tr_b8 v[88:89], v36 offset:16
	ds_read_b64_tr_b8 v[90:91], v36 offset:32
	ds_read_b64_tr_b8 v[92:93], v36 offset:48
	ds_read_b64_tr_b8 v[94:95], v36 offset:2624
	ds_read_b64_tr_b8 v[96:97], v36 offset:2640
	ds_read_b64_tr_b8 v[98:99], v36 offset:2656
	ds_read_b64_tr_b8 v[100:101], v36 offset:2672
	s_waitcnt lgkmcnt(0)
	s_waitcnt vmcnt(3)
	ds_write_b128 v37, v[38:41]
	s_waitcnt vmcnt(2)
	ds_write_b128 v37, v[42:45] offset:640
	s_waitcnt vmcnt(1)
	ds_write_b128 v37, v[46:49] offset:1312
	s_waitcnt vmcnt(0)
	ds_write_b128 v37, v[50:53] offset:1952
	v_mfma_f32_16x16x32_fp8_fp8 v[54:57], v[18:19], v[86:87], v[54:57]
	v_mfma_f32_16x16x32_fp8_fp8 v[58:61], v[18:19], v[88:89], v[58:61]
	v_mfma_f32_16x16x32_fp8_fp8 v[62:65], v[18:19], v[90:91], v[62:65]
	v_mfma_f32_16x16x32_fp8_fp8 v[66:69], v[18:19], v[92:93], v[66:69]
	v_mfma_f32_16x16x32_fp8_fp8 v[70:73], v[18:19], v[94:95], v[70:73]
	v_mfma_f32_16x16x32_fp8_fp8 v[74:77], v[18:19], v[96:97], v[74:77]
	v_mfma_f32_16x16x32_fp8_fp8 v[78:81], v[18:19], v[98:99], v[78:81]
	v_mfma_f32_16x16x32_fp8_fp8 v[82:85], v[18:19], v[100:101], v[82:85]
	s_waitcnt lgkmcnt(0)
	ds_read_b64_tr_b8 v[86:87], v36 offset:0
	ds_read_b64_tr_b8 v[88:89], v36 offset:16
	ds_read_b64_tr_b8 v[90:91], v36 offset:32
	ds_read_b64_tr_b8 v[92:93], v36 offset:48
	ds_read_b64_tr_b8 v[94:95], v36 offset:2624
	ds_read_b64_tr_b8 v[96:97], v36 offset:2640
	ds_read_b64_tr_b8 v[98:99], v36 offset:2656
	ds_read_b64_tr_b8 v[100:101], v36 offset:2672
	s_waitcnt lgkmcnt(0)
	v_mfma_f32_16x16x32_fp8_fp8 v[2:5], v[26:27], v[86:87], v[54:57]
	v_mfma_f32_16x16x32_fp8_fp8 v[6:9], v[26:27], v[88:89], v[58:61]
	v_mfma_f32_16x16x32_fp8_fp8 v[10:13], v[26:27], v[90:91], v[62:65]
	v_mfma_f32_16x16x32_fp8_fp8 v[14:17], v[26:27], v[92:93], v[66:69]
	v_mfma_f32_16x16x32_fp8_fp8 v[18:21], v[26:27], v[94:95], v[70:73]
	v_mfma_f32_16x16x32_fp8_fp8 v[22:25], v[26:27], v[96:97], v[74:77]
	v_mfma_f32_16x16x32_fp8_fp8 v[30:33], v[26:27], v[98:99], v[78:81]
	v_mfma_f32_16x16x32_fp8_fp8 v[26:29], v[26:27], v[100:101], v[82:85]
	v_div_scale_f32 v36, s[8:9], v35, v35, 1.0
	v_rcp_f32_e32 v37, v36
	v_readlane_b32 s8, v254, 62
	s_add_u32 s0, s8, s0
	v_readlane_b32 s8, v254, 63
	s_addc_u32 s1, s8, s1
	v_cmp_gt_i32_e64 s[8:9], 2, v211
	v_fma_f32 v38, -v36, v37, 1.0
	v_fmac_f32_e32 v37, v38, v37
	v_div_scale_f32 v38, vcc, 1.0, v35, 1.0
	v_mul_f32_e32 v39, v38, v37
	v_fma_f32 v40, -v36, v39, v38
	v_fmac_f32_e32 v39, v40, v37
	v_fma_f32 v36, -v36, v39, v38
	v_div_fmas_f32 v36, v36, v37, v39
	v_div_fixup_f32 v35, v36, v35, 1.0
	ds_bpermute_b32 v36, v34, v35
	ds_bpermute_b32 v37, v34, v35 offset:16
	v_cmp_eq_u32_e32 vcc, 0, v211
	s_and_saveexec_b64 s[10:11], s[8:9]
	s_cbranch_execz .LBB0_1336
	v_lshl_add_u32 v38, v211, 8, v210
	v_cndmask_b32_e32 v2, v18, v2, vcc
	s_waitcnt lgkmcnt(0)
	v_cndmask_b32_e32 v18, v37, v36, vcc
	v_mul_f32_e32 v2, v2, v18
	v_ashrrev_i32_e32 v39, 31, v38
	v_cvt_pk_bf16_f32 v2, v2, s0
	v_lshl_add_u64 v[36:37], v[38:39], 1, s[0:1]
	global_store_short v[36:37], v2, off
	v_cndmask_b32_e32 v2, v22, v6, vcc
	v_mul_f32_e32 v2, v2, v18
	v_cvt_pk_bf16_f32 v2, v2, s0
	global_store_short v[36:37], v2, off offset:32
	v_cndmask_b32_e32 v2, v30, v10, vcc
	v_mul_f32_e32 v2, v2, v18
	v_cvt_pk_bf16_f32 v2, v2, s0
	global_store_short v[36:37], v2, off offset:64
	v_cndmask_b32_e32 v2, v26, v14, vcc
	v_mul_f32_e32 v2, v2, v18
	v_cvt_pk_bf16_f32 v2, v2, s0
	global_store_short v[36:37], v2, off offset:96
